# mLSTM chunk loop: pipelined LDS fragment reads (S, Q.C, state update), next-chunk loads a full chunk ahead, global_ stores for h
# baseline (speedup 1.0000x reference)
.LBB0_734:
	s_or_b64 exec, exec, s[80:81]
	v_cndmask_b32_e64 v171, v79, v87, s[62:63]
	v_cndmask_b32_e64 v170, v78, v86, s[62:63]
	v_cndmask_b32_e64 v169, v77, v85, s[62:63]
	v_cndmask_b32_e64 v168, v76, v84, s[62:63]
	v_cndmask_b32_e64 v172, v80, v88, s[62:63]
	v_add_u32_e32 v0, s11, v131
	v_cndmask_b32_e64 v175, v83, v91, s[62:63]
	v_cndmask_b32_e64 v174, v82, v90, s[62:63]
	v_cndmask_b32_e64 v173, v81, v89, s[62:63]
	ds_write_b128 v0, v[168:171]
	ds_write_b128 v0, v[172:175] offset:1024
	v_cndmask_b32_e64 v172, v84, v76, s[62:63]
	v_add_u32_e32 v76, s21, v131
	s_waitcnt lgkmcnt(0)
	s_barrier
	v_cndmask_b32_e64 v0, v87, v79, s[62:63]
	v_cndmask_b32_e64 v3, v86, v78, s[62:63]
	v_cndmask_b32_e64 v178, v85, v77, s[62:63]
	v_cndmask_b32_e64 v179, v91, v83, s[62:63]
	v_cndmask_b32_e64 v180, v90, v82, s[62:63]
	v_cndmask_b32_e64 v181, v89, v81, s[62:63]
	v_cndmask_b32_e64 v182, v88, v80, s[62:63]
	ds_read_b128 v[80:83], v76
	ds_read_b128 v[76:79], v76 offset:1024
	ds_read_b128 v[84:87], v159
	ds_read_b128 v[88:91], v160
	ds_read_b128 v[168:171], v161
	s_waitcnt lgkmcnt(4)
	v_add_f32_e32 v80, v172, v80
	v_lshl_add_u64 v[174:175], v[104:105], 0, s[88:89]
	s_waitcnt lgkmcnt(2)
	v_fma_f32 v80, v80, v84, v92
	s_waitcnt lgkmcnt(1)
	v_max_f32_e64 v88, |v88|, |v88|
	s_waitcnt lgkmcnt(0)
	v_max_f32_e32 v84, v168, v168
	v_max_f32_e32 v84, v88, v84
	v_div_scale_f32 v88, s[80:81], v84, v84, v80
	v_rcp_f32_e32 v92, v88
	s_mov_b32 s80, 0x3a800000
	v_add_f32_e32 v3, v3, v82
	v_fma_f32 v3, v3, v86, v94
	v_fma_f32 v168, -v88, v92, 1.0
	v_fmac_f32_e32 v92, v168, v92
	v_div_scale_f32 v168, vcc, v80, v84, v80
	v_mul_f32_e32 v172, v168, v92
	v_fma_f32 v173, -v88, v172, v168
	v_fmac_f32_e32 v172, v173, v92
	v_fma_f32 v88, -v88, v172, v168
	v_div_fmas_f32 v88, v88, v92, v172
	v_div_fixup_f32 v80, v88, v84, v80
	v_add_co_u32_e32 v176, vcc, s80, v174
	v_cvt_pk_bf16_f32 v80, v80, v1
	v_max_f32_e64 v84, |v89|, |v89|
	s_nop 0
	v_addc_co_u32_e32 v177, vcc, 0, v175, vcc
	global_store_short v[176:177], v80, off
	v_add_f32_e32 v80, v178, v81
	v_max_f32_e32 v81, v169, v169
	v_fma_f32 v80, v80, v85, v93
	v_max_f32_e32 v81, v84, v81
	v_div_scale_f32 v84, s[80:81], v81, v81, v80
	v_rcp_f32_e32 v85, v84
	v_lshl_add_u64 v[172:173], v[106:107], 0, s[88:89]
	v_add_f32_e32 v0, v0, v83
	v_fmac_f32_e32 v95, v0, v87
	v_fma_f32 v88, -v84, v85, 1.0
	v_fmac_f32_e32 v85, v88, v85
	v_div_scale_f32 v88, vcc, v80, v81, v80
	v_mul_f32_e32 v89, v88, v85
	v_fma_f32 v92, -v84, v89, v88
	v_fmac_f32_e32 v89, v92, v85
	v_fma_f32 v84, -v84, v89, v88
	v_div_fmas_f32 v84, v84, v85, v89
	v_div_fixup_f32 v80, v84, v81, v80
	v_cvt_pk_bf16_f32 v84, v80, v1
	v_or_b32_e32 v80, 0x800, v172
	v_mov_b32_e32 v81, v173
	v_lshl_add_u64 v[80:81], v[102:103], 0, v[80:81]
	global_store_short v[80:81], v84, off
	v_max_f32_e32 v80, v170, v170
	v_max_f32_e64 v81, |v90|, |v90|
	v_max_f32_e32 v80, v81, v80
	v_div_scale_f32 v81, s[80:81], v80, v80, v3
	v_rcp_f32_e32 v82, v81
	v_max_f32_e32 v0, v171, v171
	v_lshl_add_u64 v[92:93], v[172:173], 0, s[96:97]
	v_fma_f32 v84, -v81, v82, 1.0
	v_fmac_f32_e32 v82, v84, v82
	v_div_scale_f32 v84, vcc, v3, v80, v3
	v_mul_f32_e32 v85, v84, v82
	v_fma_f32 v86, -v81, v85, v84
	v_fmac_f32_e32 v85, v86, v82
	v_fma_f32 v81, -v81, v85, v84
	v_div_fmas_f32 v81, v81, v82, v85
	v_div_fixup_f32 v3, v81, v80, v3
	v_or_b32_e32 v80, 0x1000, v172
	v_mov_b32_e32 v81, v173
	v_cvt_pk_bf16_f32 v3, v3, v1
	v_lshl_add_u64 v[80:81], v[102:103], 0, v[80:81]
	global_store_short v[80:81], v3, off
	v_max_f32_e64 v3, |v91|, |v91|
	v_max_f32_e32 v0, v3, v0
	v_div_scale_f32 v3, s[80:81], v0, v0, v95
	v_rcp_f32_e32 v80, v3
	s_nop 0
	v_fma_f32 v81, -v3, v80, 1.0
	v_fmac_f32_e32 v80, v81, v80
	v_div_scale_f32 v81, vcc, v95, v0, v95
	v_mul_f32_e32 v82, v81, v80
	v_fma_f32 v83, -v3, v82, v81
	v_fmac_f32_e32 v82, v83, v80
	v_fma_f32 v3, -v3, v82, v81
	v_div_fmas_f32 v3, v3, v80, v82
	v_or_b32_e32 v80, 0x1800, v172
	v_mov_b32_e32 v81, v173
	v_div_fixup_f32 v0, v3, v0, v95
	v_lshl_add_u64 v[80:81], v[102:103], 0, v[80:81]
	v_cvt_pk_bf16_f32 v0, v0, v1
	global_store_short v[80:81], v0, off
	ds_read_b128 v[80:83], v159 offset:64
	ds_read_b128 v[84:87], v160 offset:64
	ds_read_b128 v[88:91], v161 offset:64
	v_add_f32_e32 v0, v182, v76
	s_waitcnt lgkmcnt(0)
	v_fma_f32 v0, v0, v80, v72
	v_max_f32_e64 v72, |v84|, |v84|
	v_max_f32_e32 v3, v88, v88
	v_max_f32_e32 v3, v72, v3
	v_div_scale_f32 v72, s[80:81], v3, v3, v0
	v_rcp_f32_e32 v76, v72
	s_mov_b32 s80, 0x3a808000
	v_fma_f32 v80, -v72, v76, 1.0
	v_fmac_f32_e32 v76, v80, v76
	v_div_scale_f32 v80, vcc, v0, v3, v0
	v_mul_f32_e32 v84, v80, v76
	v_fma_f32 v88, -v72, v84, v80
	v_fmac_f32_e32 v84, v88, v76
	v_fma_f32 v72, -v72, v84, v80
	v_div_fmas_f32 v72, v72, v76, v84
	v_div_fixup_f32 v0, v72, v3, v0
	v_add_co_u32_e32 v94, vcc, s80, v174
	v_cvt_pk_bf16_f32 v0, v0, v1
	v_max_f32_e32 v3, v89, v89
	s_nop 0
	v_addc_co_u32_e32 v95, vcc, 0, v175, vcc
	global_store_short v[94:95], v0, off
	v_add_f32_e32 v0, v181, v77
	v_max_f32_e64 v72, |v85|, |v85|
	v_fma_f32 v0, v0, v81, v73
	v_max_f32_e32 v3, v72, v3
	v_div_scale_f32 v72, s[80:81], v3, v3, v0
	v_rcp_f32_e32 v73, v72
	v_add_u32_e32 v94, 0, v2
	v_fma_f32 v76, -v72, v73, 1.0
	v_fmac_f32_e32 v73, v76, v73
	v_div_scale_f32 v76, vcc, v0, v3, v0
	v_mul_f32_e32 v77, v76, v73
	v_fma_f32 v80, -v72, v77, v76
	v_fmac_f32_e32 v77, v80, v73
	v_fma_f32 v72, -v72, v77, v76
	v_div_fmas_f32 v72, v72, v73, v77
	v_div_fixup_f32 v0, v72, v3, v0
	v_or_b32_e32 v72, 0x800, v92
	v_mov_b32_e32 v73, v93
	v_cvt_pk_bf16_f32 v0, v0, v1
	v_lshl_add_u64 v[72:73], v[102:103], 0, v[72:73]
	global_store_short v[72:73], v0, off
	v_add_f32_e32 v0, v180, v78
	v_max_f32_e32 v3, v90, v90
	v_max_f32_e64 v72, |v86|, |v86|
	v_fma_f32 v0, v0, v82, v74
	v_max_f32_e32 v3, v72, v3
	v_div_scale_f32 v72, s[80:81], v3, v3, v0
	v_rcp_f32_e32 v73, v72
	s_nop 0
	v_fma_f32 v74, -v72, v73, 1.0
	v_fmac_f32_e32 v73, v74, v73
	v_div_scale_f32 v74, vcc, v0, v3, v0
	v_mul_f32_e32 v76, v74, v73
	v_fma_f32 v77, -v72, v76, v74
	v_fmac_f32_e32 v76, v77, v73
	v_fma_f32 v72, -v72, v76, v74
	v_div_fmas_f32 v72, v72, v73, v76
	v_div_fixup_f32 v0, v72, v3, v0
	v_or_b32_e32 v72, 0x1000, v92
	v_mov_b32_e32 v73, v93
	v_cvt_pk_bf16_f32 v0, v0, v1
	v_lshl_add_u64 v[72:73], v[102:103], 0, v[72:73]
	global_store_short v[72:73], v0, off
	v_add_f32_e32 v0, v179, v79
	v_fmac_f32_e32 v75, v0, v83
	v_max_f32_e32 v0, v91, v91
	v_max_f32_e64 v3, |v87|, |v87|
	v_max_f32_e32 v0, v3, v0
	v_div_scale_f32 v3, s[80:81], v0, v0, v75
	v_rcp_f32_e32 v72, v3
	v_or_b32_e32 v92, 0x1800, v92
	v_fma_f32 v73, -v3, v72, 1.0
	v_fmac_f32_e32 v72, v73, v72
	v_div_scale_f32 v73, vcc, v75, v0, v75
	v_mul_f32_e32 v74, v73, v72
	v_fma_f32 v76, -v3, v74, v73
	v_fmac_f32_e32 v74, v76, v72
	v_fma_f32 v3, -v3, v74, v73
	v_div_fmas_f32 v3, v3, v72, v74
	v_div_fixup_f32 v0, v3, v0, v75
	v_cvt_pk_bf16_f32 v0, v0, v1
	v_lshl_add_u64 v[72:73], v[102:103], 0, v[92:93]
	global_store_short v[72:73], v0, off
	v_mov_b32_e32 v0, s19
	ds_read_b32 v92, v0
	v_add_u32_e32 v0, 0x12c00, v167
	v_add_u32_e32 v3, 0x12e40, v167
	ds_read_b64_tr_b16 v[80:81], v0
	ds_read_b64_tr_b16 v[82:83], v3
	ds_read_b128 v[72:75], v135
	ds_read_b128 v[76:79], v135 offset:16
	v_add_u32_e32 v0, 0x13e00, v167
	v_add_u32_e32 v3, 0x14040, v167
	ds_read_b64_tr_b16 v[206:207], v0
	ds_read_b64_tr_b16 v[208:209], v3
	ds_read_b128 v[198:201], v135 offset:128
	ds_read_b128 v[202:205], v135 offset:144
	s_mov_b32 s98, 0
	s_and_b64 vcc, exec, s[28:29]
	s_cselect_b32 s98, 64, s98
	s_and_b64 vcc, exec, s[30:31]
	s_cselect_b32 s98, 0x80, s98
	s_and_b64 vcc, exec, s[34:35]
	s_cselect_b32 s98, 0xc0, s98
	v_add_u32_e32 v88, s98, v94
	ds_read_b64_tr_b16 v[168:169], v94
	ds_read_b64_tr_b16 v[170:171], v94 offset:2112
	ds_read_b64_tr_b16 v[172:173], v94 offset:32
	ds_read_b64_tr_b16 v[174:175], v94 offset:2144
	ds_read_b64_tr_b16 v[176:177], v94 offset:64
	ds_read_b64_tr_b16 v[178:179], v94 offset:2176
	s_waitcnt lgkmcnt(6)
	v_cvt_pk_bf16_f32 v84, v72, v73
	v_cvt_pk_bf16_f32 v85, v74, v75
	v_cvt_pk_bf16_f32 v86, v76, v77
	v_cvt_pk_bf16_f32 v87, v78, v79
	v_cvt_pk_bf16_f32 v194, v198, v199
	v_cvt_pk_bf16_f32 v195, v200, v201
	v_cvt_pk_bf16_f32 v196, v202, v203
	v_cvt_pk_bf16_f32 v197, v204, v205
	v_mov_b32_e32 v93, v92
	v_pk_mul_f32 v[68:69], v[68:69], v[92:93]
	v_pk_mul_f32 v[70:71], v[70:71], v[92:93]
	v_pk_mul_f32 v[64:65], v[64:65], v[92:93]
	v_pk_mul_f32 v[66:67], v[66:67], v[92:93]
	v_pk_mul_f32 v[56:57], v[56:57], v[92:93]
	v_pk_mul_f32 v[58:59], v[58:59], v[92:93]
	v_pk_mul_f32 v[60:61], v[60:61], v[92:93]
	v_pk_mul_f32 v[62:63], v[62:63], v[92:93]
	v_pk_mul_f32 v[48:49], v[48:49], v[92:93]
	v_pk_mul_f32 v[50:51], v[50:51], v[92:93]
	v_pk_mul_f32 v[52:53], v[52:53], v[92:93]
	v_pk_mul_f32 v[54:55], v[54:55], v[92:93]
	v_pk_mul_f32 v[40:41], v[40:41], v[92:93]
	v_pk_mul_f32 v[42:43], v[42:43], v[92:93]
	v_pk_mul_f32 v[44:45], v[44:45], v[92:93]
	v_pk_mul_f32 v[46:47], v[46:47], v[92:93]
	ds_read_b64_tr_b16 v[180:181], v94 offset:96
	ds_read_b64_tr_b16 v[182:183], v94 offset:2208
	ds_read_b64_tr_b16 v[184:185], v94 offset:128
	ds_read_b64_tr_b16 v[186:187], v94 offset:2240
	ds_read_b64_tr_b16 v[188:189], v94 offset:160
	ds_read_b64_tr_b16 v[190:191], v94 offset:2272
	s_waitcnt lgkmcnt(10)
	v_mfma_f32_16x16x32_bf16 v[68:71], v[168:171], v[80:83], v[68:71]
	ds_read_b64_tr_b16 v[168:169], v94 offset:192
	ds_read_b64_tr_b16 v[170:171], v94 offset:2304
	s_waitcnt lgkmcnt(10)
	v_mfma_f32_16x16x32_bf16 v[64:67], v[172:175], v[80:83], v[64:67]
	ds_read_b64_tr_b16 v[172:173], v94 offset:224
	ds_read_b64_tr_b16 v[174:175], v94 offset:2336
	s_waitcnt lgkmcnt(10)
	v_mfma_f32_16x16x32_bf16 v[56:59], v[176:179], v[80:83], v[56:59]
	ds_read_b64_tr_b16 v[176:177], v88
	ds_read_b64_tr_b16 v[178:179], v88 offset:2112
	s_waitcnt lgkmcnt(10)
	v_mfma_f32_16x16x32_bf16 v[60:63], v[180:183], v[80:83], v[60:63]
	ds_read_b64_tr_b16 v[180:181], v88 offset:32
	ds_read_b64_tr_b16 v[182:183], v88 offset:2144
	s_waitcnt lgkmcnt(10)
	v_mfma_f32_16x16x32_bf16 v[48:51], v[184:187], v[80:83], v[48:51]
	ds_read_b64_tr_b16 v[184:185], v94 offset:16896
	ds_read_b64_tr_b16 v[186:187], v94 offset:19008
	s_waitcnt lgkmcnt(10)
	v_mfma_f32_16x16x32_bf16 v[52:55], v[188:191], v[80:83], v[52:55]
	ds_read_b64_tr_b16 v[188:189], v94 offset:16928
	ds_read_b64_tr_b16 v[190:191], v94 offset:19040
	s_waitcnt lgkmcnt(10)
	v_mfma_f32_16x16x32_bf16 v[40:43], v[168:171], v[80:83], v[40:43]
	ds_read_b64_tr_b16 v[168:169], v94 offset:16960
	ds_read_b64_tr_b16 v[170:171], v94 offset:19072
	s_waitcnt lgkmcnt(10)
	v_mfma_f32_16x16x32_bf16 v[44:47], v[172:175], v[80:83], v[44:47]
	ds_read_b64_tr_b16 v[172:173], v94 offset:16992
	ds_read_b64_tr_b16 v[174:175], v94 offset:19104
	s_waitcnt lgkmcnt(10)
	v_mfma_f32_16x16x32_bf16 v[72:75], v[176:179], v[84:87], 0
	ds_read_b64_tr_b16 v[176:177], v94 offset:17024
	ds_read_b64_tr_b16 v[178:179], v94 offset:19136
	s_waitcnt lgkmcnt(10)
	v_mfma_f32_16x16x32_bf16 v[76:79], v[180:183], v[84:87], 0
	ds_read_b64_tr_b16 v[180:181], v94 offset:17056
	ds_read_b64_tr_b16 v[182:183], v94 offset:19168
	s_waitcnt lgkmcnt(10)
	v_mfma_f32_16x16x32_bf16 v[68:71], v[184:187], v[206:209], v[68:71]
	ds_read_b64_tr_b16 v[184:185], v94 offset:17088
	ds_read_b64_tr_b16 v[186:187], v94 offset:19200
	s_waitcnt lgkmcnt(10)
	v_mfma_f32_16x16x32_bf16 v[64:67], v[188:191], v[206:209], v[64:67]
	ds_read_b64_tr_b16 v[188:189], v94 offset:17120
	ds_read_b64_tr_b16 v[190:191], v94 offset:19232
	s_waitcnt lgkmcnt(10)
	v_mfma_f32_16x16x32_bf16 v[56:59], v[168:171], v[206:209], v[56:59]
	ds_read_b64_tr_b16 v[168:169], v88 offset:16896
	ds_read_b64_tr_b16 v[170:171], v88 offset:19008
	s_waitcnt lgkmcnt(10)
	v_mfma_f32_16x16x32_bf16 v[60:63], v[172:175], v[206:209], v[60:63]
	ds_read_b64_tr_b16 v[172:173], v88 offset:16928
	ds_read_b64_tr_b16 v[174:175], v88 offset:19040
	s_waitcnt lgkmcnt(10)
	v_mfma_f32_16x16x32_bf16 v[48:51], v[176:179], v[206:209], v[48:51]
	s_waitcnt lgkmcnt(8)
	v_mfma_f32_16x16x32_bf16 v[52:55], v[180:183], v[206:209], v[52:55]
	s_waitcnt lgkmcnt(6)
	v_mfma_f32_16x16x32_bf16 v[40:43], v[184:187], v[206:209], v[40:43]
	s_waitcnt lgkmcnt(4)
	v_mfma_f32_16x16x32_bf16 v[44:47], v[188:191], v[206:209], v[44:47]
	s_waitcnt lgkmcnt(2)
	v_mfma_f32_16x16x32_bf16 v[72:75], v[168:171], v[194:197], v[72:75]
	s_waitcnt lgkmcnt(0)
	v_mfma_f32_16x16x32_bf16 v[76:79], v[172:175], v[194:197], v[76:79]
	s_and_saveexec_b64 s[80:81], s[60:61]
	s_cbranch_execz .LBB0_725
	ds_read_b128 v[80:83], v154
	ds_read_b128 v[84:87], v154 offset:64
	s_nop 7
	s_waitcnt lgkmcnt(1)
	v_pk_fma_f32 v[74:75], v[92:93], v[82:83], v[74:75]
	v_pk_fma_f32 v[72:73], v[92:93], v[80:81], v[72:73]
	s_waitcnt lgkmcnt(0)
	v_pk_fma_f32 v[78:79], v[92:93], v[86:87], v[78:79]
	v_pk_fma_f32 v[76:77], v[92:93], v[84:85], v[76:77]
	ds_write_b128 v154, v[72:75]
	ds_write_b128 v154, v[76:79] offset:64
	s_branch .LBB0_725
